# code placement (sec 9.3): the 8 GEMM K-loop heads and the attention loop head aligned to 64 B, on top of flips deleted + static prio for waves 0-3
# baseline (speedup 1.0000x reference)
.LBB0_544:
	v_mov_b64_e32 v[2:3], 0x659
	s_ashr_i32 s25, s24, 31
	v_cmp_lt_i64_e32 vcc, s[26:27], v[2:3]
	s_lshl_b64 s[26:27], s[24:25], 19
	s_add_u32 s26, s94, s26
	s_addc_u32 s27, s95, s27
	s_and_b64 s[28:29], vcc, exec
	s_cselect_b32 s25, s27, s31
	s_cselect_b32 s43, s26, s30
	s_ashr_i32 s23, s22, 31
	s_lshl_b64 s[28:29], s[22:23], 19
	s_add_u32 s28, s4, s28
	s_addc_u32 s29, s5, s29
	s_and_b64 s[36:37], vcc, exec
	s_cselect_b32 s23, s29, s35
	s_cselect_b32 s44, s28, s34
	s_add_u32 s30, s30, 0x40080
	s_addc_u32 s31, s31, 0
	s_add_u32 s45, s34, 0x100
	v_mov_b32_e32 v2, 0
	s_addc_u32 s46, s35, 0
	s_mov_b32 s47, -2
	v_mov_b32_e32 v3, v2
	v_mov_b32_e32 v4, v2
	v_mov_b32_e32 v5, v2
	v_mov_b32_e32 v6, v2
	v_mov_b32_e32 v7, v2
	v_mov_b32_e32 v8, v2
	v_mov_b32_e32 v9, v2
	v_mov_b32_e32 v10, v2
	v_mov_b32_e32 v11, v2
	v_mov_b32_e32 v12, v2
	v_mov_b32_e32 v13, v2
	v_mov_b32_e32 v14, v2
	v_mov_b32_e32 v15, v2
	v_mov_b32_e32 v16, v2
	v_mov_b32_e32 v17, v2
	v_mov_b32_e32 v18, v2
	v_mov_b32_e32 v19, v2
	v_mov_b32_e32 v20, v2
	v_mov_b32_e32 v21, v2
	v_mov_b32_e32 v22, v2
	v_mov_b32_e32 v23, v2
	v_mov_b32_e32 v24, v2
	v_mov_b32_e32 v25, v2
	v_mov_b32_e32 v26, v2
	v_mov_b32_e32 v27, v2
	v_mov_b32_e32 v28, v2
	v_mov_b32_e32 v29, v2
	v_mov_b32_e32 v30, v2
	v_mov_b32_e32 v31, v2
	v_mov_b32_e32 v32, v2
	v_mov_b32_e32 v33, v2
	v_mov_b32_e32 v34, v2
	v_mov_b32_e32 v35, v2
	v_mov_b32_e32 v36, v2
	v_mov_b32_e32 v37, v2
	v_mov_b32_e32 v38, v2
	v_mov_b32_e32 v39, v2
	v_mov_b32_e32 v40, v2
	v_mov_b32_e32 v41, v2
	v_mov_b32_e32 v42, v2
	v_mov_b32_e32 v43, v2
	v_mov_b32_e32 v44, v2
	v_mov_b32_e32 v45, v2
	v_mov_b32_e32 v46, v2
	v_mov_b32_e32 v47, v2
	v_mov_b32_e32 v48, v2
	v_mov_b32_e32 v49, v2
	v_mov_b32_e32 v50, v2
	v_mov_b32_e32 v51, v2
	v_mov_b32_e32 v52, v2
	v_mov_b32_e32 v53, v2
	v_mov_b32_e32 v54, v2
	v_mov_b32_e32 v55, v2
	v_mov_b32_e32 v56, v2
	v_mov_b32_e32 v57, v2
	v_mov_b32_e32 v58, v2
	v_mov_b32_e32 v59, v2
	v_mov_b32_e32 v60, v2
	v_mov_b32_e32 v61, v2
	v_mov_b32_e32 v62, v2
	v_mov_b32_e32 v63, v2
	v_mov_b32_e32 v64, v2
	v_mov_b32_e32 v65, v2
	v_mov_b32_e32 v66, v2
	v_mov_b32_e32 v67, v2
	v_mov_b32_e32 v68, v2
	v_mov_b32_e32 v69, v2
	v_mov_b32_e32 v70, v2
	v_mov_b32_e32 v71, v2
	v_mov_b32_e32 v72, v2
	v_mov_b32_e32 v73, v2
	v_mov_b32_e32 v74, v2
	v_mov_b32_e32 v75, v2
	v_mov_b32_e32 v76, v2
	v_mov_b32_e32 v77, v2
	v_mov_b32_e32 v78, v2
	v_mov_b32_e32 v79, v2
	v_mov_b32_e32 v80, v2
	v_mov_b32_e32 v81, v2
	v_mov_b32_e32 v82, v2
	v_mov_b32_e32 v83, v2
	v_mov_b32_e32 v84, v2
	v_mov_b32_e32 v85, v2
	v_mov_b32_e32 v86, v2
	v_mov_b32_e32 v87, v2
	v_mov_b32_e32 v88, v2
	v_mov_b32_e32 v89, v2
	v_mov_b32_e32 v90, v2
	v_mov_b32_e32 v91, v2
	v_mov_b32_e32 v92, v2
	v_mov_b32_e32 v93, v2
	v_mov_b32_e32 v94, v2
	v_mov_b32_e32 v95, v2
	v_mov_b32_e32 v96, v2
	v_mov_b32_e32 v97, v2
	v_mov_b32_e32 v100, v2
	v_mov_b32_e32 v101, v2
	v_mov_b32_e32 v102, v2
	v_mov_b32_e32 v103, v2
	v_mov_b32_e32 v104, v2
	v_mov_b32_e32 v105, v2
	v_mov_b32_e32 v106, v2
	v_mov_b32_e32 v107, v2
	v_mov_b32_e32 v108, v2
	v_mov_b32_e32 v109, v2
	v_mov_b32_e32 v110, v2
	v_mov_b32_e32 v111, v2
	v_mov_b32_e32 v112, v2
	v_mov_b32_e32 v113, v2
	v_mov_b32_e32 v114, v2
	v_mov_b32_e32 v115, v2
	v_mov_b32_e32 v116, v2
	v_mov_b32_e32 v117, v2
	v_mov_b32_e32 v118, v2
	v_mov_b32_e32 v119, v2
	v_mov_b32_e32 v120, v2
	v_mov_b32_e32 v121, v2
	v_mov_b32_e32 v122, v2
	v_mov_b32_e32 v123, v2
	v_mov_b32_e32 v124, v2
	v_mov_b32_e32 v125, v2
	v_mov_b32_e32 v126, v2
	v_mov_b32_e32 v127, v2
	v_mov_b32_e32 v128, v2
	v_mov_b32_e32 v129, v2
	v_mov_b32_e32 v130, v2
	v_mov_b32_e32 v131, v2
	.p2align	6

.LBB0_689:
	s_add_u32 s42, s26, 0x100
	v_mov_b32_e32 v2, 0
	s_addc_u32 s43, s27, 0
	s_mov_b32 s44, -2
	v_mov_b32_e32 v3, v2
	v_mov_b32_e32 v4, v2
	v_mov_b32_e32 v5, v2
	v_mov_b32_e32 v6, v2
	v_mov_b32_e32 v7, v2
	v_mov_b32_e32 v8, v2
	v_mov_b32_e32 v9, v2
	v_mov_b32_e32 v14, v2
	v_mov_b32_e32 v15, v2
	v_mov_b32_e32 v16, v2
	v_mov_b32_e32 v17, v2
	v_mov_b32_e32 v22, v2
	v_mov_b32_e32 v23, v2
	v_mov_b32_e32 v24, v2
	v_mov_b32_e32 v25, v2
	v_mov_b32_e32 v30, v2
	v_mov_b32_e32 v31, v2
	v_mov_b32_e32 v32, v2
	v_mov_b32_e32 v33, v2
	v_mov_b32_e32 v38, v2
	v_mov_b32_e32 v39, v2
	v_mov_b32_e32 v40, v2
	v_mov_b32_e32 v41, v2
	v_mov_b32_e32 v46, v2
	v_mov_b32_e32 v47, v2
	v_mov_b32_e32 v48, v2
	v_mov_b32_e32 v49, v2
	v_mov_b32_e32 v54, v2
	v_mov_b32_e32 v55, v2
	v_mov_b32_e32 v56, v2
	v_mov_b32_e32 v57, v2
	v_mov_b32_e32 v10, v2
	v_mov_b32_e32 v11, v2
	v_mov_b32_e32 v12, v2
	v_mov_b32_e32 v13, v2
	v_mov_b32_e32 v18, v2
	v_mov_b32_e32 v19, v2
	v_mov_b32_e32 v20, v2
	v_mov_b32_e32 v21, v2
	v_mov_b32_e32 v26, v2
	v_mov_b32_e32 v27, v2
	v_mov_b32_e32 v28, v2
	v_mov_b32_e32 v29, v2
	v_mov_b32_e32 v34, v2
	v_mov_b32_e32 v35, v2
	v_mov_b32_e32 v36, v2
	v_mov_b32_e32 v37, v2
	v_mov_b32_e32 v42, v2
	v_mov_b32_e32 v43, v2
	v_mov_b32_e32 v44, v2
	v_mov_b32_e32 v45, v2
	v_mov_b32_e32 v50, v2
	v_mov_b32_e32 v51, v2
	v_mov_b32_e32 v52, v2
	v_mov_b32_e32 v53, v2
	v_mov_b32_e32 v58, v2
	v_mov_b32_e32 v59, v2
	v_mov_b32_e32 v60, v2
	v_mov_b32_e32 v61, v2
	v_mov_b32_e32 v62, v2
	v_mov_b32_e32 v63, v2
	v_mov_b32_e32 v64, v2
	v_mov_b32_e32 v65, v2
	v_mov_b32_e32 v66, v2
	v_mov_b32_e32 v67, v2
	v_mov_b32_e32 v68, v2
	v_mov_b32_e32 v69, v2
	v_mov_b32_e32 v70, v2
	v_mov_b32_e32 v71, v2
	v_mov_b32_e32 v72, v2
	v_mov_b32_e32 v73, v2
	v_mov_b32_e32 v82, v2
	v_mov_b32_e32 v83, v2
	v_mov_b32_e32 v84, v2
	v_mov_b32_e32 v85, v2
	v_mov_b32_e32 v86, v2
	v_mov_b32_e32 v87, v2
	v_mov_b32_e32 v88, v2
	v_mov_b32_e32 v89, v2
	v_mov_b32_e32 v100, v2
	v_mov_b32_e32 v101, v2
	v_mov_b32_e32 v102, v2
	v_mov_b32_e32 v103, v2
	v_mov_b32_e32 v104, v2
	v_mov_b32_e32 v105, v2
	v_mov_b32_e32 v106, v2
	v_mov_b32_e32 v107, v2
	v_mov_b32_e32 v116, v2
	v_mov_b32_e32 v117, v2
	v_mov_b32_e32 v118, v2
	v_mov_b32_e32 v119, v2
	v_mov_b32_e32 v120, v2
	v_mov_b32_e32 v121, v2
	v_mov_b32_e32 v122, v2
	v_mov_b32_e32 v123, v2
	v_mov_b32_e32 v74, v2
	v_mov_b32_e32 v75, v2
	v_mov_b32_e32 v76, v2
	v_mov_b32_e32 v77, v2
	v_mov_b32_e32 v78, v2
	v_mov_b32_e32 v79, v2
	v_mov_b32_e32 v80, v2
	v_mov_b32_e32 v81, v2
	v_mov_b32_e32 v90, v2
	v_mov_b32_e32 v91, v2
	v_mov_b32_e32 v92, v2
	v_mov_b32_e32 v93, v2
	v_mov_b32_e32 v94, v2
	v_mov_b32_e32 v95, v2
	v_mov_b32_e32 v96, v2
	v_mov_b32_e32 v97, v2
	v_mov_b32_e32 v108, v2
	v_mov_b32_e32 v109, v2
	v_mov_b32_e32 v110, v2
	v_mov_b32_e32 v111, v2
	v_mov_b32_e32 v112, v2
	v_mov_b32_e32 v113, v2
	v_mov_b32_e32 v114, v2
	v_mov_b32_e32 v115, v2
	v_mov_b32_e32 v124, v2
	v_mov_b32_e32 v125, v2
	v_mov_b32_e32 v126, v2
	v_mov_b32_e32 v127, v2
	v_mov_b32_e32 v128, v2
	v_mov_b32_e32 v129, v2
	v_mov_b32_e32 v130, v2
	v_mov_b32_e32 v131, v2
	.p2align	6

.LBB0_1343:
	s_and_b32 s3, s21, 3
	s_and_b64 s[4:5], exec, s[34:35]
	s_cselect_b32 s3, -1, s3
	s_cmp_eq_u32 s3, 2
	s_movk_i32 s4, 0x3080
	s_cselect_b32 s4, 0x2000, s4
	s_cmp_lg_u32 s3, 1
	s_cselect_b32 s4, s4, 0x1000
	s_cmp_gt_i32 s3, 0
	s_cselect_b32 s8, s4, 0
	s_mul_i32 s18, s8, 0xe00
	v_readlane_b32 s4, v253, 7
	v_readlane_b32 s5, v253, 8
	s_add_u32 s4, s4, s18
	v_lshlrev_b32_e32 v2, 8, v181
	v_mov_b32_e32 v3, v99
	v_lshl_add_u32 v7, v7, 7, v14
	s_addc_u32 s5, s5, 0
	v_lshlrev_b64 v[50:51], 1, v[2:3]
	v_cvt_pk_bf16_f32 v5, v5, v99
	ds_write_b16 v7, v5
	v_cvt_pk_bf16_f32 v4, v4, v99
	v_lshl_add_u64 v[2:3], s[4:5], 0, v[50:51]
	ds_write_b16 v7, v4 offset:32
	v_ashrrev_i32_e32 v4, 4, v6
	v_lshlrev_b32_e32 v5, 3, v6
	s_movk_i32 s4, 0x700
	v_and_b32_e32 v7, 0x78, v5
	v_mul_lo_u32 v8, v4, s4
	v_or_b32_e32 v8, v8, v7
	v_lshlrev_b32_e32 v52, 1, v8
	v_readfirstlane_b32 s4, v2
	v_readfirstlane_b32 s5, v3
	s_waitcnt lgkmcnt(0)
	s_barrier
	v_add_u32_e32 v54, 0x1c000, v52
	s_nop 1
	global_load_dwordx4 v[8:11], v52, s[4:5] offset:1792
	global_load_dwordx4 v[14:17], v54, s[4:5] offset:1792
	s_lshl_b32 s22, s8, 7
	v_readlane_b32 s8, v253, 5
	v_lshlrev_b32_e32 v26, 4, v6
	v_readlane_b32 s9, v253, 6
	s_add_u32 s24, s8, s22
	v_ashrrev_i32_e32 v13, 3, v6
	v_and_b32_e32 v30, 0x70, v26
	s_addc_u32 s25, s9, 0
	v_lshl_or_b32 v56, v13, 7, v30
	global_load_dwordx4 v[18:21], v52, s[4:5] offset:1536
	global_load_dwordx4 v[22:25], v54, s[4:5] offset:1536
	global_load_dwordx4 v[26:29], v56, s[24:25]
	v_lshlrev_b32_e32 v31, 7, v194
	v_lshlrev_b32_e32 v12, 1, v12
	v_readlane_b32 s4, v255, 34
	v_lshlrev_b32_e32 v32, 1, v4
	v_lshrrev_b32_e32 v33, 1, v4
	v_add3_u32 v12, s4, v31, v12
	v_and_b32_e32 v31, 0xfffff0, v4
	v_and_b32_e32 v35, 3, v4
	v_add_u32_e32 v36, 32, v4
	s_add_i32 s4, 0, 0x14000
	ds_read_b128 v[144:147], v12
	ds_read_b128 v[140:143], v12 offset:32
	ds_read_b128 v[136:139], v12 offset:64
	ds_read_b128 v[132:135], v12 offset:96
	v_and_or_b32 v12, v32, 8, v31
	v_and_or_b32 v31, v33, 4, v35
	v_and_b32_e32 v32, 0xfffff0, v36
	v_lshlrev_b32_e32 v33, 1, v36
	s_and_b64 s[0:1], s[0:1], exec
	v_bfe_u32 v34, v5, 5, 2
	v_lshrrev_b32_e32 v12, 1, v12
	v_and_or_b32 v32, v33, 8, v32
	s_cselect_b32 s5, 0x104, 4
	s_cmp_lt_u32 s3, 2
	v_lshlrev_b32_e32 v7, 1, v7
	v_or_b32_e32 v12, v12, v34
	v_lshrrev_b32_e32 v32, 1, v32
	s_cselect_b32 s3, 64, 0x42
	s_and_b64 s[0:1], exec, s[34:35]
	v_lshlrev_b32_e32 v31, 6, v31
	v_and_b32_e32 v35, 48, v7
	v_lshlrev_b32_e32 v12, 9, v12
	v_or_b32_e32 v32, v32, v34
	s_cselect_b32 s3, s5, s3
	s_add_i32 s0, 0, 0x8000
	v_lshlrev_b32_e32 v32, 9, v32
	v_or3_b32 v12, v12, v31, v35
	s_cmp_lg_u32 s0, -1
	v_or3_b32 v31, v32, v31, v35
	v_add_u32_e32 v205, 0, v12
	s_cselect_b32 s0, s0, 0
	s_movk_i32 s8, 0x70
	v_add_u32_e32 v206, 0, v31
	s_waitcnt vmcnt(0)
	v_mov_b32_e32 v12, s0
	s_movk_i32 s0, 0x180
	v_mul_lo_u32 v4, v4, s0
	v_bitop3_b32 v37, v98, v5, s8 bitop3:0x78
	s_waitcnt vmcnt(4)
	ds_write_b128 v205, v[8:11]
	s_waitcnt vmcnt(3)
	ds_write_b128 v206, v[14:17]
	v_lshrrev_b32_e32 v8, 1, v6
	v_bitop3_b32 v7, v7, v8, s8 bitop3:0x78
	v_add3_u32 v207, v7, v4, 0
	v_mul_lo_u32 v4, v13, s0
	v_or_b32_e32 v7, 0x100, v30
	v_and_b32_e32 v8, 0x70, v6
	v_mad_u32_u24 v53, v195, s0, v12
	v_xad_u32 v4, v7, v8, v4
	v_add_u32_e32 v201, v37, v53
	v_add_u32_e32 v208, 0, v4
	s_waitcnt vmcnt(2)
	ds_write_b128 v207, v[18:21] offset:32768
	s_waitcnt vmcnt(1)
	ds_write_b128 v207, v[22:25] offset:45056
	s_waitcnt vmcnt(0)
	ds_write_b128 v208, v[26:29] offset:32768
	s_waitcnt lgkmcnt(0)
	s_barrier
	ds_read_b128 v[8:11], v201
	ds_read_b128 v[12:15], v201 offset:128
	s_waitcnt lgkmcnt(1)
	v_mfma_f32_32x32x16_bf16 v[18:33], v[8:11], v[128:131], 0
	ds_read_b128 v[8:11], v201 offset:12288
	ds_read_b128 v[60:63], v201 offset:256
	v_and_b32_e32 v4, 0x70, v5
	v_bitop3_b32 v5, v98, v4, 32 bitop3:0x36
	v_add_u32_e32 v203, v5, v53
	v_bitop3_b32 v5, v98, v4, 64 bitop3:0x36
	v_add_u32_e32 v204, v5, v53
	s_waitcnt lgkmcnt(1)
	v_mfma_f32_32x32x16_bf16 v[34:49], v[8:11], v[128:131], 0
	ds_read_b128 v[8:11], v203
	ds_read_b128 v[64:67], v203 offset:128
	ds_read_b128 v[68:71], v203 offset:256
	s_movk_i32 s0, 0x60
	v_bitop3_b32 v4, v98, v4, s0 bitop3:0x36
	v_add_u32_e32 v202, v4, v53
	s_mov_b64 s[0:1], 0x38700
	v_lshl_add_u64 v[4:5], v[2:3], 0, s[0:1]
	s_waitcnt lgkmcnt(2)
	v_mfma_f32_32x32x16_bf16 v[18:33], v[8:11], v[124:127], v[18:33]
	ds_read_b128 v[8:11], v203 offset:12288
	s_mov_b64 s[0:1], 0x38600
	v_lshl_add_u64 v[2:3], v[2:3], 0, s[0:1]
	v_readfirstlane_b32 s0, v4
	v_readfirstlane_b32 s1, v5
	v_readfirstlane_b32 s8, v2
	v_readfirstlane_b32 s9, v3
	s_waitcnt lgkmcnt(0)
	v_mfma_f32_32x32x16_bf16 v[34:49], v[8:11], v[124:127], v[34:49]
	ds_read_b128 v[8:11], v204
	ds_read_b128 v[72:75], v204 offset:128
	ds_read_b128 v[76:79], v204 offset:256
	v_mov_b32_e32 v57, v99
	v_add_u32_e32 v209, 0x3000, v207
	s_cmp_lg_u32 0, -1
	v_lshlrev_b32_e32 v4, 1, v58
	v_and_b32_e32 v4, 32, v4
	s_waitcnt lgkmcnt(2)
	v_mfma_f32_32x32x16_bf16 v[18:33], v[8:11], v[120:123], v[18:33]
	ds_read_b128 v[8:11], v204 offset:12288
	s_mov_b32 s36, s63
	s_mov_b32 s37, s63
	s_mov_b32 s19, s63
	s_mov_b32 s38, s63
	s_mov_b32 s39, s63
	s_mov_b32 s40, s63
	s_waitcnt lgkmcnt(0)
	v_mfma_f32_32x32x16_bf16 v[34:49], v[8:11], v[120:123], v[34:49]
	ds_read_b128 v[8:11], v202
	ds_read_b128 v[80:83], v202 offset:128
	s_mov_b32 s41, s63
	s_mov_b32 s42, s63
	s_mov_b32 s43, s63
	s_mov_b32 s44, s63
	s_mov_b32 s45, s63
	s_mov_b32 s46, s63
	s_waitcnt lgkmcnt(1)
	v_mfma_f32_32x32x16_bf16 v[18:33], v[8:11], v[116:119], v[18:33]
	ds_read_b128 v[8:11], v202 offset:12288
	ds_read_b128 v[84:87], v202 offset:256
	s_mov_b32 s47, s63
	s_mov_b32 s48, s63
	s_mov_b32 s49, s63
	s_mov_b32 s50, s63
	s_mov_b32 s51, s63
	s_mov_b32 s23, s63
	v_mfma_f32_32x32x16_bf16 v[18:33], v[12:15], v[112:115], v[18:33]
	v_mov_b32_e32 v53, v99
	v_mov_b32_e32 v55, v99
	v_lshl_add_u64 v[182:183], s[22:23], 0, v[56:57]
	v_mov_b32_e32 v227, 0x3200
	v_mov_b32_e32 v199, 0
	s_waitcnt lgkmcnt(1)
	v_mfma_f32_32x32x16_bf16 v[34:49], v[8:11], v[116:119], v[34:49]
	ds_read_b128 v[8:11], v201 offset:12416
	ds_read_b128 v[12:15], v201 offset:12544
	v_mfma_f32_32x32x16_bf16 v[18:33], v[64:67], v[108:111], v[18:33]
	s_waitcnt lgkmcnt(1)
	v_mfma_f32_32x32x16_bf16 v[34:49], v[8:11], v[112:115], v[34:49]
	ds_read_b128 v[8:11], v203 offset:12416
	ds_read_b128 v[64:67], v203 offset:12544
	v_mfma_f32_32x32x16_bf16 v[18:33], v[72:75], v[104:107], v[18:33]
	s_waitcnt lgkmcnt(1)
	v_mfma_f32_32x32x16_bf16 v[34:49], v[8:11], v[108:111], v[34:49]
	ds_read_b128 v[8:11], v204 offset:12416
	ds_read_b128 v[72:75], v204 offset:12544
	v_mfma_f32_32x32x16_bf16 v[18:33], v[80:83], v[100:103], v[18:33]
	s_waitcnt lgkmcnt(1)
	v_mfma_f32_32x32x16_bf16 v[34:49], v[8:11], v[104:107], v[34:49]
	ds_read_b128 v[8:11], v202 offset:12416
	ds_read_b128 v[80:83], v202 offset:12544
	v_mfma_f32_32x32x16_bf16 v[18:33], v[60:63], v[144:147], v[18:33]
	global_load_dwordx4 v[60:63], v54, s[0:1]
	global_load_dwordx4 v[88:91], v52, s[8:9]
	global_load_dwordx4 v[92:95], v52, s[0:1]
	global_load_dwordx4 v[148:151], v54, s[8:9]
	s_movk_i32 s0, 0x2000
	s_mov_b32 s8, 2
	s_waitcnt lgkmcnt(1)
	v_mfma_f32_32x32x16_bf16 v[34:49], v[8:11], v[100:103], v[34:49]
	v_lshl_add_u64 v[8:9], s[24:25], 0, v[56:57]
	v_add_co_u32_e32 v2, vcc, s0, v8
	v_cmp_gt_u32_e64 s[0:1], 32, v58
	s_nop 0
	v_addc_co_u32_e32 v3, vcc, 0, v9, vcc
	global_load_dwordx4 v[152:155], v[2:3], off
	v_mfma_f32_32x32x16_bf16 v[18:33], v[68:71], v[140:143], v[18:33]
	s_waitcnt vmcnt(0)
	s_waitcnt vmcnt(2)
	ds_write_b128 v205, v[92:95] offset:16384
	ds_write_b128 v206, v[60:63] offset:16384
	ds_write_b128 v207, v[88:91] offset:57344
	s_waitcnt vmcnt(1)
	ds_write_b128 v209, v[148:151] offset:57344
	s_waitcnt vmcnt(0)
	ds_write_b128 v208, v[152:155] offset:57344
	v_mfma_f32_32x32x16_bf16 v[34:49], v[12:15], v[144:147], v[34:49]
	v_and_b32_e32 v2, 0x3fffffc0, v6
	v_lshl_add_u32 v196, v2, 2, s4
	s_cselect_b32 s4, 0, 0
	v_lshlrev_b32_e32 v3, 4, v58
	v_lshlrev_b32_e32 v2, 3, v58
	v_and_b32_e32 v3, 0xc0, v3
	v_and_or_b32 v3, v2, 24, v3
	v_mfma_f32_32x32x16_bf16 v[18:33], v[76:79], v[136:139], v[18:33]
	v_and_b32_e32 v2, 0x100, v2
	v_or3_b32 v59, v3, v4, v2
	v_mov_b64_e32 v[2:3], s[36:37]
	v_add_u32_e32 v200, s4, v59
	v_mov_b64_e32 v[16:17], s[50:51]
	v_mov_b64_e32 v[4:5], s[38:39]
	v_mov_b64_e32 v[6:7], s[40:41]
	v_mfma_f32_32x32x16_bf16 v[34:49], v[64:67], v[140:143], v[34:49]
	v_mov_b64_e32 v[8:9], s[42:43]
	v_mov_b64_e32 v[10:11], s[44:45]
	v_mov_b64_e32 v[12:13], s[46:47]
	v_mov_b64_e32 v[14:15], s[48:49]
	v_lshl_add_u32 v197, v195, 2, v196
	s_waitcnt lgkmcnt(0)
	s_barrier
	v_mfma_f32_32x32x16_bf16 v[18:33], v[84:87], v[132:135], v[18:33]
	v_mfma_f32_32x32x16_bf16 v[34:49], v[72:75], v[136:139], v[34:49]
	s_nop 10
	v_max_f32_e32 v64, v19, v19
	v_max_f32_e32 v65, v18, v18
	v_max_f32_e32 v64, v65, v64
	v_max3_f32 v64, v64, v20, v21
	v_max3_f32 v64, v64, v22, v23
	v_max3_f32 v64, v64, v24, v25
	v_max3_f32 v64, v64, v26, v27
	v_mfma_f32_32x32x16_bf16 v[34:49], v[80:83], v[132:135], v[34:49]
	v_max3_f32 v64, v64, v28, v29
	v_max3_f32 v64, v64, v30, v31
	v_max3_f32 v64, v64, v32, v33
	s_nop 8
	v_max3_f32 v64, v64, v34, v35
	v_max3_f32 v64, v64, v36, v37
	v_max3_f32 v64, v64, v38, v39
	v_max3_f32 v64, v64, v40, v41
	v_max3_f32 v64, v64, v42, v43
	v_max3_f32 v64, v64, v44, v45
	v_max3_f32 v64, v64, v46, v47
	v_max3_f32 v64, v64, v48, v49
	v_mov_b32_e32 v65, v64
	s_nop 1
	v_permlane32_swap_b32_e32 v64, v65
	v_max_f32_e32 v65, v65, v65
	v_max_f32_e32 v64, v64, v64
	v_max_f32_e32 v64, v64, v65
	v_max_f32_e32 v60, 0xf149f2ca, v64
	v_sub_f32_e32 v61, 0xf149f2ca, v60
	v_mul_f32_e32 v61, 0x3dd53b94, v61
	v_add_f32_e32 v65, 0x7149f2ca, v64
	v_exp_f32_e32 v61, v61
	v_cmp_ge_f32_e32 vcc, s11, v65
	s_cmp_eq_u64 vcc, exec
	s_cselect_b64 vcc, -1, 0
	v_cndmask_b32_e64 v210, v61, 1.0, vcc
	v_mov_b32_e32 v61, 0xf149f2ca
	v_cndmask_b32_e32 v211, v60, v61, vcc
	v_mul_f32_e32 v60, 0xbdd53b94, v211
	v_fmamk_f32 v18, v18, 0x3dd53b94, v60
	v_exp_f32_e32 v169, v18
	v_fmamk_f32 v18, v19, 0x3dd53b94, v60
	v_exp_f32_e32 v191, v18
	v_fmamk_f32 v18, v20, 0x3dd53b94, v60
	v_exp_f32_e32 v170, v18
	v_fmamk_f32 v18, v21, 0x3dd53b94, v60
	v_exp_f32_e32 v192, v18
	v_fmamk_f32 v18, v22, 0x3dd53b94, v60
	v_exp_f32_e32 v190, v18
	v_fmamk_f32 v18, v23, 0x3dd53b94, v60
	v_exp_f32_e32 v193, v18
	v_fmamk_f32 v18, v24, 0x3dd53b94, v60
	v_exp_f32_e32 v171, v18
	v_fmamk_f32 v18, v25, 0x3dd53b94, v60
	v_exp_f32_e32 v189, v18
	v_fmamk_f32 v18, v26, 0x3dd53b94, v60
	v_exp_f32_e32 v173, v18
	v_fmamk_f32 v18, v27, 0x3dd53b94, v60
	v_exp_f32_e32 v175, v18
	v_fmamk_f32 v18, v28, 0x3dd53b94, v60
	v_exp_f32_e32 v174, v18
	v_fmamk_f32 v18, v29, 0x3dd53b94, v60
	v_exp_f32_e32 v188, v18
	v_fmamk_f32 v18, v30, 0x3dd53b94, v60
	v_exp_f32_e32 v164, v18
	v_fmamk_f32 v18, v31, 0x3dd53b94, v60
	v_pk_fma_f32 v[148:149], v[48:49], s[56:57], v[60:61] op_sel_hi:[1,0,0]
	v_pk_fma_f32 v[154:155], v[46:47], s[56:57], v[60:61] op_sel_hi:[1,0,0]
	v_pk_fma_f32 v[158:159], v[44:45], s[56:57], v[60:61] op_sel_hi:[1,0,0]
	v_pk_fma_f32 v[150:151], v[42:43], s[56:57], v[60:61] op_sel_hi:[1,0,0]
	v_pk_fma_f32 v[152:153], v[40:41], s[56:57], v[60:61] op_sel_hi:[1,0,0]
	v_pk_fma_f32 v[156:157], v[38:39], s[56:57], v[60:61] op_sel_hi:[1,0,0]
	v_pk_fma_f32 v[160:161], v[36:37], s[56:57], v[60:61] op_sel_hi:[1,0,0]
	v_pk_fma_f32 v[162:163], v[34:35], s[56:57], v[60:61] op_sel_hi:[1,0,0]
	v_exp_f32_e32 v166, v18
	v_fmamk_f32 v18, v32, 0x3dd53b94, v60
	v_fmac_f32_e32 v60, 0x3dd53b94, v33
	v_exp_f32_e32 v165, v18
	v_exp_f32_e32 v167, v60
	s_addk_i32 s4, 0x4000
	v_lshl_add_u64 v[18:19], s[18:19], 0, v[50:51]
	v_add_u32_e32 v198, s4, v59
	v_lshl_add_u64 v[184:185], v[18:19], 0, v[54:55]
	v_lshl_add_u64 v[186:187], v[18:19], 0, v[52:53]
	v_mov_b64_e32 v[64:65], v[16:17]
	v_mov_b64_e32 v[48:49], v[16:17]
	v_mov_b64_e32 v[32:33], v[16:17]
	v_mov_b64_e32 v[62:63], v[14:15]
	v_mov_b64_e32 v[60:61], v[12:13]
	v_mov_b64_e32 v[58:59], v[10:11]
	v_mov_b64_e32 v[56:57], v[8:9]
	v_mov_b64_e32 v[54:55], v[6:7]
	v_mov_b64_e32 v[52:53], v[4:5]
	v_mov_b64_e32 v[50:51], v[2:3]
	v_mov_b64_e32 v[46:47], v[14:15]
	v_mov_b64_e32 v[44:45], v[12:13]
	v_mov_b64_e32 v[42:43], v[10:11]
	v_mov_b64_e32 v[40:41], v[8:9]
	v_mov_b64_e32 v[38:39], v[6:7]
	v_mov_b64_e32 v[36:37], v[4:5]
	v_mov_b64_e32 v[34:35], v[2:3]
	v_mov_b64_e32 v[30:31], v[14:15]
	v_mov_b64_e32 v[28:29], v[12:13]
	v_mov_b64_e32 v[26:27], v[10:11]
	v_mov_b64_e32 v[24:25], v[8:9]
	v_mov_b64_e32 v[22:23], v[6:7]
	v_mov_b64_e32 v[20:21], v[4:5]
	v_mov_b64_e32 v[18:19], v[2:3]
	v_and_b32_e32 v230, 63, v0
	v_lshrrev_b32_e32 v231, 6, v0
	v_lshrrev_b32_e32 v232, 4, v0
	v_mul_u32_u24_e32 v232, 0xe00, v232
	v_and_b32_e32 v233, 15, v0
	v_lshl_add_u32 v232, v233, 4, v232
	v_sub_u32_e32 v232, v186, v232
	v_lshrrev_b32_e32 v233, 3, v0
	v_and_b32_e32 v236, 7, v0
	v_lshlrev_b32_e32 v236, 4, v236
	v_lshl_add_u32 v233, v233, 7, v236
	v_sub_u32_e32 v233, v182, v233
	v_add_u32_e32 v232, 0x39d1dc00, v232
	v_add_u32_e32 v233, 0x39b15600, v233
	v_mov_b32_e32 v243, 0
	v_mov_b32_e32 v244, 0x2000
	v_mov_b32_e32 v245, 0x38000
	v_bfe_u32 v236, v230, 2, 3
	v_lshl_add_u32 v236, v231, 3, v236
	v_and_b32_e32 v237, 0xfffffff3, v236
	v_and_b32_e32 v238, 4, v236
	v_lshl_or_b32 v237, v238, 1, v237
	v_and_b32_e32 v238, 8, v236
	v_lshrrev_b32_e32 v238, 1, v238
	v_or_b32_e32 v237, v237, v238
	v_add_u32_e32 v237, 64, v237
	v_mul_u32_u24_e32 v237, 0xe00, v237
	v_add_u32_e32 v237, v237, v232
	v_lshrrev_b32_e32 v238, 5, v230
	v_lshlrev_b32_e32 v238, 6, v238
	v_and_b32_e32 v239, 3, v230
	v_lshl_add_u32 v238, v239, 4, v238
	v_add_u32_e32 v237, v237, v238
	v_add_u32_e32 v242, 0x100, v237
	v_lshl_add_u64 v[206:207], s[14:15], 0, v[242:243]
	v_mov_b32_e32 v236, v230
	v_mul_u32_u24_e32 v237, 0x2ab, v236
	v_lshrrev_b32_e32 v237, 14, v237
	v_mul_u32_u24_e32 v238, 24, v237
	v_sub_u32_e32 v238, v236, v238
	v_lshl_add_u32 v237, v231, 3, v237
	v_bfe_u32 v239, v237, 1, 3
	v_xor_b32_e32 v238, v238, v239
	v_add_u32_e32 v237, 0x80, v237
	v_mul_u32_u24_e32 v240, 0xe00, v237
	v_add_u32_e32 v240, v240, v232
	v_lshl_add_u32 v240, v238, 4, v240
	v_lshl_add_u32 v241, v237, 7, v233
	v_lshl_add_u32 v241, v238, 4, v241
	v_subrev_u32_e32 v241, 0x100, v241
	v_cmp_gt_u32_e32 vcc, 16, v238
	s_nop 1
	v_cndmask_b32_e32 v242, v241, v240, vcc
	v_cndmask_b32_e32 v205, v244, v245, vcc
	v_lshl_add_u64 v[182:183], s[14:15], 0, v[242:243]
	v_add_u32_e32 v236, 0x40, v230
	v_mul_u32_u24_e32 v237, 0x2ab, v236
	v_lshrrev_b32_e32 v237, 14, v237
	v_mul_u32_u24_e32 v238, 24, v237
	v_sub_u32_e32 v238, v236, v238
	v_lshl_add_u32 v237, v231, 3, v237
	v_bfe_u32 v239, v237, 1, 3
	v_xor_b32_e32 v238, v238, v239
	v_add_u32_e32 v237, 0x80, v237
	v_mul_u32_u24_e32 v240, 0xe00, v237
	v_add_u32_e32 v240, v240, v232
	v_lshl_add_u32 v240, v238, 4, v240
	v_lshl_add_u32 v241, v237, 7, v233
	v_lshl_add_u32 v241, v238, 4, v241
	v_subrev_u32_e32 v241, 0x100, v241
	v_cmp_gt_u32_e32 vcc, 16, v238
	s_nop 1
	v_cndmask_b32_e32 v242, v241, v240, vcc
	v_cndmask_b32_e32 v208, v244, v245, vcc
	v_lshl_add_u64 v[184:185], s[14:15], 0, v[242:243]
	v_add_u32_e32 v236, 0x80, v230
	v_mul_u32_u24_e32 v237, 0x2ab, v236
	v_lshrrev_b32_e32 v237, 14, v237
	v_mul_u32_u24_e32 v238, 24, v237
	v_sub_u32_e32 v238, v236, v238
	v_lshl_add_u32 v237, v231, 3, v237
	v_bfe_u32 v239, v237, 1, 3
	v_xor_b32_e32 v238, v238, v239
	v_add_u32_e32 v237, 0x80, v237
	v_mul_u32_u24_e32 v240, 0xe00, v237
	v_add_u32_e32 v240, v240, v232
	v_lshl_add_u32 v240, v238, 4, v240
	v_lshl_add_u32 v241, v237, 7, v233
	v_lshl_add_u32 v241, v238, 4, v241
	v_subrev_u32_e32 v241, 0x100, v241
	v_cmp_gt_u32_e32 vcc, 16, v238
	s_nop 1
	v_cndmask_b32_e32 v242, v241, v240, vcc
	v_cndmask_b32_e32 v209, v244, v245, vcc
	v_lshl_add_u64 v[186:187], s[14:15], 0, v[242:243]
	.p2align	6

.LBB0_1591:
	v_mov_b64_e32 v[2:3], 0x200
	s_ashr_i32 s25, s24, 31
	v_cmp_lt_i64_e32 vcc, s[26:27], v[2:3]
	s_lshl_b64 s[26:27], s[24:25], 20
	s_add_u32 s26, s49, s26
	s_addc_u32 s27, s50, s27
	s_and_b64 s[28:29], vcc, exec
	s_cselect_b32 s25, s27, s31
	s_cselect_b32 s41, s26, s30
	s_ashr_i32 s19, s18, 31
	s_lshl_b64 s[28:29], s[18:19], 20
	s_add_u32 s28, s51, s28
	s_addc_u32 s29, s52, s29
	s_and_b64 s[36:37], vcc, exec
	s_cselect_b32 s19, s29, s35
	s_cselect_b32 s42, s28, s34
	s_add_u32 s30, s30, 0x80080
	s_addc_u32 s31, s31, 0
	s_add_u32 s43, s34, 0x100
	v_mov_b32_e32 v2, 0
	s_addc_u32 s44, s35, 0
	s_mov_b32 s45, -2
	v_mov_b32_e32 v3, v2
	v_mov_b32_e32 v4, v2
	v_mov_b32_e32 v5, v2
	v_mov_b32_e32 v6, v2
	v_mov_b32_e32 v7, v2
	v_mov_b32_e32 v8, v2
	v_mov_b32_e32 v9, v2
	v_mov_b32_e32 v10, v2
	v_mov_b32_e32 v11, v2
	v_mov_b32_e32 v12, v2
	v_mov_b32_e32 v13, v2
	v_mov_b32_e32 v14, v2
	v_mov_b32_e32 v15, v2
	v_mov_b32_e32 v16, v2
	v_mov_b32_e32 v17, v2
	v_mov_b32_e32 v34, v2
	v_mov_b32_e32 v35, v2
	v_mov_b32_e32 v36, v2
	v_mov_b32_e32 v37, v2
	v_mov_b32_e32 v38, v2
	v_mov_b32_e32 v39, v2
	v_mov_b32_e32 v40, v2
	v_mov_b32_e32 v41, v2
	v_mov_b32_e32 v50, v2
	v_mov_b32_e32 v51, v2
	v_mov_b32_e32 v52, v2
	v_mov_b32_e32 v53, v2
	v_mov_b32_e32 v54, v2
	v_mov_b32_e32 v55, v2
	v_mov_b32_e32 v56, v2
	v_mov_b32_e32 v57, v2
	v_mov_b32_e32 v18, v2
	v_mov_b32_e32 v19, v2
	v_mov_b32_e32 v20, v2
	v_mov_b32_e32 v21, v2
	v_mov_b32_e32 v22, v2
	v_mov_b32_e32 v23, v2
	v_mov_b32_e32 v24, v2
	v_mov_b32_e32 v25, v2
	v_mov_b32_e32 v26, v2
	v_mov_b32_e32 v27, v2
	v_mov_b32_e32 v28, v2
	v_mov_b32_e32 v29, v2
	v_mov_b32_e32 v30, v2
	v_mov_b32_e32 v31, v2
	v_mov_b32_e32 v32, v2
	v_mov_b32_e32 v33, v2
	v_mov_b32_e32 v42, v2
	v_mov_b32_e32 v43, v2
	v_mov_b32_e32 v44, v2
	v_mov_b32_e32 v45, v2
	v_mov_b32_e32 v46, v2
	v_mov_b32_e32 v47, v2
	v_mov_b32_e32 v48, v2
	v_mov_b32_e32 v49, v2
	v_mov_b32_e32 v58, v2
	v_mov_b32_e32 v59, v2
	v_mov_b32_e32 v60, v2
	v_mov_b32_e32 v61, v2
	v_mov_b32_e32 v62, v2
	v_mov_b32_e32 v63, v2
	v_mov_b32_e32 v64, v2
	v_mov_b32_e32 v65, v2
	v_mov_b32_e32 v66, v2
	v_mov_b32_e32 v67, v2
	v_mov_b32_e32 v68, v2
	v_mov_b32_e32 v69, v2
	v_mov_b32_e32 v74, v2
	v_mov_b32_e32 v75, v2
	v_mov_b32_e32 v76, v2
	v_mov_b32_e32 v77, v2
	v_mov_b32_e32 v100, v2
	v_mov_b32_e32 v101, v2
	v_mov_b32_e32 v102, v2
	v_mov_b32_e32 v103, v2
	v_mov_b32_e32 v104, v2
	v_mov_b32_e32 v105, v2
	v_mov_b32_e32 v106, v2
	v_mov_b32_e32 v107, v2
	v_mov_b32_e32 v116, v2
	v_mov_b32_e32 v117, v2
	v_mov_b32_e32 v118, v2
	v_mov_b32_e32 v119, v2
	v_mov_b32_e32 v120, v2
	v_mov_b32_e32 v121, v2
	v_mov_b32_e32 v122, v2
	v_mov_b32_e32 v123, v2
	v_mov_b32_e32 v132, v2
	v_mov_b32_e32 v133, v2
	v_mov_b32_e32 v134, v2
	v_mov_b32_e32 v135, v2
	v_mov_b32_e32 v136, v2
	v_mov_b32_e32 v137, v2
	v_mov_b32_e32 v138, v2
	v_mov_b32_e32 v139, v2
	v_mov_b32_e32 v90, v2
	v_mov_b32_e32 v91, v2
	v_mov_b32_e32 v92, v2
	v_mov_b32_e32 v93, v2
	v_mov_b32_e32 v94, v2
	v_mov_b32_e32 v95, v2
	v_mov_b32_e32 v96, v2
	v_mov_b32_e32 v97, v2
	v_mov_b32_e32 v108, v2
	v_mov_b32_e32 v109, v2
	v_mov_b32_e32 v110, v2
	v_mov_b32_e32 v111, v2
	v_mov_b32_e32 v112, v2
	v_mov_b32_e32 v113, v2
	v_mov_b32_e32 v114, v2
	v_mov_b32_e32 v115, v2
	v_mov_b32_e32 v124, v2
	v_mov_b32_e32 v125, v2
	v_mov_b32_e32 v126, v2
	v_mov_b32_e32 v127, v2
	v_mov_b32_e32 v128, v2
	v_mov_b32_e32 v129, v2
	v_mov_b32_e32 v130, v2
	v_mov_b32_e32 v131, v2
	v_mov_b32_e32 v140, v2
	v_mov_b32_e32 v141, v2
	v_mov_b32_e32 v142, v2
	v_mov_b32_e32 v143, v2
	v_mov_b32_e32 v144, v2
	v_mov_b32_e32 v145, v2
	v_mov_b32_e32 v146, v2
	v_mov_b32_e32 v147, v2
	.p2align	6

.LBB0_1615:
	s_ashr_i32 s27, s26, 31
	s_xor_b64 s[30:31], s[44:45], -1
	s_lshl_b64 s[28:29], s[26:27], 20
	v_readlane_b32 s34, v252, 63
	v_readlane_b32 s35, v253, 0
	s_add_u32 s25, s34, s28
	s_addc_u32 s27, s35, s29
	s_ashr_i32 s1, s0, 31
	s_lshl_b64 s[34:35], s[0:1], 7
	s_add_u32 s28, s25, s34
	s_addc_u32 s29, s27, s35
	s_and_b64 s[48:49], s[44:45], exec
	s_cselect_b32 s1, s29, s41
	s_cselect_b32 s27, s28, s40
	s_ashr_i32 s25, s24, 31
	s_lshl_b64 s[48:49], s[24:25], 20
	s_add_u32 s25, s84, s48
	s_addc_u32 s39, s85, s49
	s_add_u32 s34, s25, s34
	s_addc_u32 s35, s39, s35
	s_and_b64 s[44:45], s[44:45], exec
	s_cselect_b32 s25, s35, s43
	s_cselect_b32 s39, s34, s42
	s_add_i32 s47, s46, -2
	s_add_u32 s40, s40, 0x80080
	s_addc_u32 s41, s41, 0
	s_add_u32 s48, s42, 0x100
	v_mov_b32_e32 v2, 0
	s_addc_u32 s49, s43, 0
	s_mov_b32 s42, 0
	v_mov_b32_e32 v3, v2
	v_mov_b32_e32 v4, v2
	v_mov_b32_e32 v5, v2
	v_mov_b32_e32 v6, v2
	v_mov_b32_e32 v7, v2
	v_mov_b32_e32 v8, v2
	v_mov_b32_e32 v9, v2
	v_mov_b32_e32 v10, v2
	v_mov_b32_e32 v11, v2
	v_mov_b32_e32 v12, v2
	v_mov_b32_e32 v13, v2
	v_mov_b32_e32 v14, v2
	v_mov_b32_e32 v15, v2
	v_mov_b32_e32 v16, v2
	v_mov_b32_e32 v17, v2
	v_mov_b32_e32 v22, v2
	v_mov_b32_e32 v23, v2
	v_mov_b32_e32 v24, v2
	v_mov_b32_e32 v25, v2
	v_mov_b32_e32 v30, v2
	v_mov_b32_e32 v31, v2
	v_mov_b32_e32 v32, v2
	v_mov_b32_e32 v33, v2
	v_mov_b32_e32 v38, v2
	v_mov_b32_e32 v39, v2
	v_mov_b32_e32 v40, v2
	v_mov_b32_e32 v41, v2
	v_mov_b32_e32 v46, v2
	v_mov_b32_e32 v47, v2
	v_mov_b32_e32 v48, v2
	v_mov_b32_e32 v49, v2
	v_mov_b32_e32 v18, v2
	v_mov_b32_e32 v19, v2
	v_mov_b32_e32 v20, v2
	v_mov_b32_e32 v21, v2
	v_mov_b32_e32 v26, v2
	v_mov_b32_e32 v27, v2
	v_mov_b32_e32 v28, v2
	v_mov_b32_e32 v29, v2
	v_mov_b32_e32 v34, v2
	v_mov_b32_e32 v35, v2
	v_mov_b32_e32 v36, v2
	v_mov_b32_e32 v37, v2
	v_mov_b32_e32 v42, v2
	v_mov_b32_e32 v43, v2
	v_mov_b32_e32 v44, v2
	v_mov_b32_e32 v45, v2
	v_mov_b32_e32 v50, v2
	v_mov_b32_e32 v51, v2
	v_mov_b32_e32 v52, v2
	v_mov_b32_e32 v53, v2
	v_mov_b32_e32 v54, v2
	v_mov_b32_e32 v55, v2
	v_mov_b32_e32 v56, v2
	v_mov_b32_e32 v57, v2
	v_mov_b32_e32 v58, v2
	v_mov_b32_e32 v59, v2
	v_mov_b32_e32 v60, v2
	v_mov_b32_e32 v61, v2
	v_mov_b32_e32 v62, v2
	v_mov_b32_e32 v63, v2
	v_mov_b32_e32 v64, v2
	v_mov_b32_e32 v65, v2
	v_mov_b32_e32 v66, v2
	v_mov_b32_e32 v67, v2
	v_mov_b32_e32 v68, v2
	v_mov_b32_e32 v69, v2
	v_mov_b32_e32 v70, v2
	v_mov_b32_e32 v71, v2
	v_mov_b32_e32 v72, v2
	v_mov_b32_e32 v73, v2
	v_mov_b32_e32 v74, v2
	v_mov_b32_e32 v75, v2
	v_mov_b32_e32 v76, v2
	v_mov_b32_e32 v77, v2
	v_mov_b32_e32 v78, v2
	v_mov_b32_e32 v79, v2
	v_mov_b32_e32 v80, v2
	v_mov_b32_e32 v81, v2
	v_mov_b32_e32 v86, v2
	v_mov_b32_e32 v87, v2
	v_mov_b32_e32 v88, v2
	v_mov_b32_e32 v89, v2
	v_mov_b32_e32 v94, v2
	v_mov_b32_e32 v95, v2
	v_mov_b32_e32 v96, v2
	v_mov_b32_e32 v97, v2
	v_mov_b32_e32 v104, v2
	v_mov_b32_e32 v105, v2
	v_mov_b32_e32 v106, v2
	v_mov_b32_e32 v107, v2
	v_mov_b32_e32 v112, v2
	v_mov_b32_e32 v113, v2
	v_mov_b32_e32 v114, v2
	v_mov_b32_e32 v115, v2
	v_mov_b32_e32 v82, v2
	v_mov_b32_e32 v83, v2
	v_mov_b32_e32 v84, v2
	v_mov_b32_e32 v85, v2
	v_mov_b32_e32 v90, v2
	v_mov_b32_e32 v91, v2
	v_mov_b32_e32 v92, v2
	v_mov_b32_e32 v93, v2
	v_mov_b32_e32 v100, v2
	v_mov_b32_e32 v101, v2
	v_mov_b32_e32 v102, v2
	v_mov_b32_e32 v103, v2
	v_mov_b32_e32 v108, v2
	v_mov_b32_e32 v109, v2
	v_mov_b32_e32 v110, v2
	v_mov_b32_e32 v111, v2
	v_mov_b32_e32 v116, v2
	v_mov_b32_e32 v117, v2
	v_mov_b32_e32 v118, v2
	v_mov_b32_e32 v119, v2
	v_mov_b32_e32 v120, v2
	v_mov_b32_e32 v121, v2
	v_mov_b32_e32 v122, v2
	v_mov_b32_e32 v123, v2
	v_mov_b32_e32 v124, v2
	v_mov_b32_e32 v125, v2
	v_mov_b32_e32 v126, v2
	v_mov_b32_e32 v127, v2
	v_mov_b32_e32 v128, v2
	v_mov_b32_e32 v129, v2
	v_mov_b32_e32 v130, v2
	v_mov_b32_e32 v131, v2
	.p2align	6

.LBB0_1869:
	v_readlane_b32 s26, v254, 17
	v_mov_b32_e32 v141, v99
	v_mov_b32_e32 v143, v99
	s_add_u32 s31, s36, 0x100
	v_readlane_b32 s27, v254, 18
	v_mov_b32_e32 v2, 0
	s_addc_u32 s20, s37, 0
	v_lshl_add_u64 v[144:145], s[26:27], 0, v[140:141]
	v_lshl_add_u64 v[146:147], s[26:27], 0, v[142:143]
	s_mov_b32 s42, -2
	s_mov_b64 s[26:27], 0
	v_mov_b32_e32 v3, v2
	v_mov_b32_e32 v4, v2
	s_waitcnt lgkmcnt(0)
	v_mov_b32_e32 v5, v2
	v_mov_b32_e32 v6, v2
	v_mov_b32_e32 v7, v2
	v_mov_b32_e32 v8, v2
	v_mov_b32_e32 v9, v2
	v_mov_b32_e32 v18, v2
	v_mov_b32_e32 v19, v2
	v_mov_b32_e32 v20, v2
	v_mov_b32_e32 v21, v2
	v_mov_b32_e32 v22, v2
	v_mov_b32_e32 v23, v2
	v_mov_b32_e32 v24, v2
	v_mov_b32_e32 v25, v2
	v_mov_b32_e32 v34, v2
	v_mov_b32_e32 v35, v2
	v_mov_b32_e32 v36, v2
	v_mov_b32_e32 v37, v2
	v_mov_b32_e32 v38, v2
	v_mov_b32_e32 v39, v2
	v_mov_b32_e32 v40, v2
	v_mov_b32_e32 v41, v2
	v_mov_b32_e32 v50, v2
	v_mov_b32_e32 v51, v2
	v_mov_b32_e32 v52, v2
	v_mov_b32_e32 v53, v2
	v_mov_b32_e32 v54, v2
	v_mov_b32_e32 v55, v2
	v_mov_b32_e32 v56, v2
	v_mov_b32_e32 v57, v2
	v_mov_b32_e32 v10, v2
	v_mov_b32_e32 v11, v2
	v_mov_b32_e32 v12, v2
	v_mov_b32_e32 v13, v2
	v_mov_b32_e32 v14, v2
	v_mov_b32_e32 v15, v2
	v_mov_b32_e32 v16, v2
	v_mov_b32_e32 v17, v2
	v_mov_b32_e32 v26, v2
	v_mov_b32_e32 v27, v2
	v_mov_b32_e32 v28, v2
	v_mov_b32_e32 v29, v2
	v_mov_b32_e32 v30, v2
	v_mov_b32_e32 v31, v2
	v_mov_b32_e32 v32, v2
	v_mov_b32_e32 v33, v2
	v_mov_b32_e32 v42, v2
	v_mov_b32_e32 v43, v2
	v_mov_b32_e32 v44, v2
	v_mov_b32_e32 v45, v2
	v_mov_b32_e32 v46, v2
	v_mov_b32_e32 v47, v2
	v_mov_b32_e32 v48, v2
	v_mov_b32_e32 v49, v2
	v_mov_b32_e32 v58, v2
	v_mov_b32_e32 v59, v2
	v_mov_b32_e32 v60, v2
	v_mov_b32_e32 v61, v2
	v_mov_b32_e32 v62, v2
	v_mov_b32_e32 v63, v2
	v_mov_b32_e32 v64, v2
	v_mov_b32_e32 v65, v2
	v_mov_b32_e32 v66, v2
	v_mov_b32_e32 v67, v2
	v_mov_b32_e32 v68, v2
	v_mov_b32_e32 v69, v2
	v_mov_b32_e32 v70, v2
	v_mov_b32_e32 v71, v2
	v_mov_b32_e32 v72, v2
	v_mov_b32_e32 v73, v2
	v_mov_b32_e32 v82, v2
	v_mov_b32_e32 v83, v2
	v_mov_b32_e32 v84, v2
	v_mov_b32_e32 v85, v2
	v_mov_b32_e32 v86, v2
	v_mov_b32_e32 v87, v2
	v_mov_b32_e32 v88, v2
	v_mov_b32_e32 v89, v2
	v_mov_b32_e32 v100, v2
	v_mov_b32_e32 v101, v2
	v_mov_b32_e32 v102, v2
	v_mov_b32_e32 v103, v2
	v_mov_b32_e32 v104, v2
	v_mov_b32_e32 v105, v2
	v_mov_b32_e32 v106, v2
	v_mov_b32_e32 v107, v2
	v_mov_b32_e32 v116, v2
	v_mov_b32_e32 v117, v2
	v_mov_b32_e32 v118, v2
	v_mov_b32_e32 v119, v2
	v_mov_b32_e32 v124, v2
	v_mov_b32_e32 v125, v2
	v_mov_b32_e32 v126, v2
	v_mov_b32_e32 v127, v2
	v_mov_b32_e32 v74, v2
	v_mov_b32_e32 v75, v2
	v_mov_b32_e32 v76, v2
	v_mov_b32_e32 v77, v2
	v_mov_b32_e32 v78, v2
	v_mov_b32_e32 v79, v2
	v_mov_b32_e32 v80, v2
	v_mov_b32_e32 v81, v2
	v_mov_b32_e32 v90, v2
	v_mov_b32_e32 v91, v2
	v_mov_b32_e32 v92, v2
	v_mov_b32_e32 v93, v2
	v_mov_b32_e32 v94, v2
	v_mov_b32_e32 v95, v2
	v_mov_b32_e32 v96, v2
	v_mov_b32_e32 v97, v2
	v_mov_b32_e32 v108, v2
	v_mov_b32_e32 v109, v2
	v_mov_b32_e32 v110, v2
	v_mov_b32_e32 v111, v2
	v_mov_b32_e32 v112, v2
	v_mov_b32_e32 v113, v2
	v_mov_b32_e32 v114, v2
	v_mov_b32_e32 v115, v2
	v_mov_b32_e32 v120, v2
	v_mov_b32_e32 v121, v2
	v_mov_b32_e32 v122, v2
	v_mov_b32_e32 v123, v2
	v_mov_b32_e32 v128, v2
	v_mov_b32_e32 v129, v2
	v_mov_b32_e32 v130, v2
	v_mov_b32_e32 v131, v2
	.p2align	6

.LBB0_2009:
	s_add_u32 s71, s34, 0x100
	v_mov_b32_e32 v2, 0
	s_addc_u32 s93, s35, 0
	s_mov_b32 vcc_lo, -2
	v_mov_b32_e32 v3, v2
	v_mov_b32_e32 v4, v2
	v_mov_b32_e32 v5, v2
	v_mov_b32_e32 v6, v2
	v_mov_b32_e32 v7, v2
	v_mov_b32_e32 v8, v2
	v_mov_b32_e32 v9, v2
	v_mov_b32_e32 v10, v2
	v_mov_b32_e32 v11, v2
	v_mov_b32_e32 v12, v2
	v_mov_b32_e32 v13, v2
	v_mov_b32_e32 v14, v2
	v_mov_b32_e32 v15, v2
	v_mov_b32_e32 v16, v2
	v_mov_b32_e32 v17, v2
	v_mov_b32_e32 v18, v2
	v_mov_b32_e32 v19, v2
	v_mov_b32_e32 v20, v2
	v_mov_b32_e32 v21, v2
	v_mov_b32_e32 v22, v2
	v_mov_b32_e32 v23, v2
	v_mov_b32_e32 v24, v2
	v_mov_b32_e32 v25, v2
	v_mov_b32_e32 v26, v2
	v_mov_b32_e32 v27, v2
	v_mov_b32_e32 v28, v2
	v_mov_b32_e32 v29, v2
	v_mov_b32_e32 v30, v2
	v_mov_b32_e32 v31, v2
	v_mov_b32_e32 v32, v2
	v_mov_b32_e32 v33, v2
	v_mov_b32_e32 v34, v2
	v_mov_b32_e32 v35, v2
	v_mov_b32_e32 v36, v2
	v_mov_b32_e32 v37, v2
	v_mov_b32_e32 v38, v2
	v_mov_b32_e32 v39, v2
	v_mov_b32_e32 v40, v2
	v_mov_b32_e32 v41, v2
	v_mov_b32_e32 v42, v2
	v_mov_b32_e32 v43, v2
	v_mov_b32_e32 v44, v2
	v_mov_b32_e32 v45, v2
	v_mov_b32_e32 v46, v2
	v_mov_b32_e32 v47, v2
	v_mov_b32_e32 v48, v2
	v_mov_b32_e32 v49, v2
	v_mov_b32_e32 v50, v2
	v_mov_b32_e32 v51, v2
	v_mov_b32_e32 v52, v2
	v_mov_b32_e32 v53, v2
	v_mov_b32_e32 v54, v2
	v_mov_b32_e32 v55, v2
	v_mov_b32_e32 v56, v2
	v_mov_b32_e32 v57, v2
	v_mov_b32_e32 v58, v2
	v_mov_b32_e32 v59, v2
	v_mov_b32_e32 v60, v2
	v_mov_b32_e32 v61, v2
	v_mov_b32_e32 v62, v2
	v_mov_b32_e32 v63, v2
	v_mov_b32_e32 v64, v2
	v_mov_b32_e32 v65, v2
	v_mov_b32_e32 v66, v2
	v_mov_b32_e32 v67, v2
	v_mov_b32_e32 v68, v2
	v_mov_b32_e32 v69, v2
	v_mov_b32_e32 v70, v2
	v_mov_b32_e32 v71, v2
	v_mov_b32_e32 v72, v2
	v_mov_b32_e32 v73, v2
	v_mov_b32_e32 v74, v2
	v_mov_b32_e32 v75, v2
	v_mov_b32_e32 v76, v2
	v_mov_b32_e32 v77, v2
	v_mov_b32_e32 v78, v2
	v_mov_b32_e32 v79, v2
	v_mov_b32_e32 v80, v2
	v_mov_b32_e32 v81, v2
	v_mov_b32_e32 v82, v2
	v_mov_b32_e32 v83, v2
	v_mov_b32_e32 v84, v2
	v_mov_b32_e32 v85, v2
	v_mov_b32_e32 v86, v2
	v_mov_b32_e32 v87, v2
	v_mov_b32_e32 v88, v2
	v_mov_b32_e32 v89, v2
	v_mov_b32_e32 v90, v2
	v_mov_b32_e32 v91, v2
	v_mov_b32_e32 v92, v2
	v_mov_b32_e32 v93, v2
	v_mov_b32_e32 v94, v2
	v_mov_b32_e32 v95, v2
	v_mov_b32_e32 v96, v2
	v_mov_b32_e32 v97, v2
	v_mov_b32_e32 v100, v2
	v_mov_b32_e32 v101, v2
	v_mov_b32_e32 v102, v2
	v_mov_b32_e32 v103, v2
	v_mov_b32_e32 v104, v2
	v_mov_b32_e32 v105, v2
	v_mov_b32_e32 v106, v2
	v_mov_b32_e32 v107, v2
	v_mov_b32_e32 v108, v2
	v_mov_b32_e32 v109, v2
	v_mov_b32_e32 v110, v2
	v_mov_b32_e32 v111, v2
	v_mov_b32_e32 v112, v2
	v_mov_b32_e32 v113, v2
	v_mov_b32_e32 v114, v2
	v_mov_b32_e32 v115, v2
	v_mov_b32_e32 v116, v2
	v_mov_b32_e32 v117, v2
	v_mov_b32_e32 v118, v2
	v_mov_b32_e32 v119, v2
	v_mov_b32_e32 v120, v2
	v_mov_b32_e32 v121, v2
	v_mov_b32_e32 v122, v2
	v_mov_b32_e32 v123, v2
	v_mov_b32_e32 v124, v2
	v_mov_b32_e32 v125, v2
	v_mov_b32_e32 v126, v2
	v_mov_b32_e32 v127, v2
	v_mov_b32_e32 v128, v2
	v_mov_b32_e32 v129, v2
	v_mov_b32_e32 v130, v2
	v_mov_b32_e32 v131, v2
	.p2align	6

.LBB0_2087:
	v_mov_b64_e32 v[2:3], 0xb2c
	s_ashr_i32 s27, s26, 31
	v_cmp_lt_i64_e32 vcc, s[28:29], v[2:3]
	s_lshl_b64 s[28:29], s[26:27], 19
	s_add_u32 s28, s94, s28
	s_addc_u32 s29, s95, s29
	s_and_b64 s[30:31], vcc, exec
	s_cselect_b32 s8, s29, s39
	s_cselect_b32 s27, s28, s38
	s_ashr_i32 s25, s24, 31
	s_lshl_b64 s[30:31], s[24:25], 19
	s_add_u32 s30, s70, s30
	s_addc_u32 s31, s71, s31
	s_and_b64 s[42:43], vcc, exec
	s_cselect_b32 s25, s31, s41
	s_cselect_b32 s35, s30, s40
	s_add_u32 s38, s38, 0x40080
	s_addc_u32 s39, s39, 0
	s_add_u32 s37, s40, 0x100
	v_mov_b32_e32 v2, 0
	s_addc_u32 s44, s41, 0
	s_mov_b32 s45, -2
	v_mov_b32_e32 v3, v2
	v_mov_b32_e32 v4, v2
	s_waitcnt lgkmcnt(0)
	v_mov_b32_e32 v5, v2
	v_mov_b32_e32 v6, v2
	v_mov_b32_e32 v7, v2
	v_mov_b32_e32 v8, v2
	v_mov_b32_e32 v9, v2
	v_mov_b32_e32 v18, v2
	v_mov_b32_e32 v19, v2
	v_mov_b32_e32 v20, v2
	v_mov_b32_e32 v21, v2
	v_mov_b32_e32 v22, v2
	v_mov_b32_e32 v23, v2
	v_mov_b32_e32 v24, v2
	v_mov_b32_e32 v25, v2
	v_mov_b32_e32 v34, v2
	v_mov_b32_e32 v35, v2
	v_mov_b32_e32 v36, v2
	v_mov_b32_e32 v37, v2
	v_mov_b32_e32 v38, v2
	v_mov_b32_e32 v39, v2
	v_mov_b32_e32 v40, v2
	v_mov_b32_e32 v41, v2
	v_mov_b32_e32 v50, v2
	v_mov_b32_e32 v51, v2
	v_mov_b32_e32 v52, v2
	v_mov_b32_e32 v53, v2
	v_mov_b32_e32 v54, v2
	v_mov_b32_e32 v55, v2
	v_mov_b32_e32 v56, v2
	v_mov_b32_e32 v57, v2
	v_mov_b32_e32 v10, v2
	v_mov_b32_e32 v11, v2
	v_mov_b32_e32 v12, v2
	v_mov_b32_e32 v13, v2
	v_mov_b32_e32 v14, v2
	v_mov_b32_e32 v15, v2
	v_mov_b32_e32 v16, v2
	v_mov_b32_e32 v17, v2
	v_mov_b32_e32 v26, v2
	v_mov_b32_e32 v27, v2
	v_mov_b32_e32 v28, v2
	v_mov_b32_e32 v29, v2
	v_mov_b32_e32 v30, v2
	v_mov_b32_e32 v31, v2
	v_mov_b32_e32 v32, v2
	v_mov_b32_e32 v33, v2
	v_mov_b32_e32 v42, v2
	v_mov_b32_e32 v43, v2
	v_mov_b32_e32 v44, v2
	v_mov_b32_e32 v45, v2
	v_mov_b32_e32 v46, v2
	v_mov_b32_e32 v47, v2
	v_mov_b32_e32 v48, v2
	v_mov_b32_e32 v49, v2
	v_mov_b32_e32 v58, v2
	v_mov_b32_e32 v59, v2
	v_mov_b32_e32 v60, v2
	v_mov_b32_e32 v61, v2
	v_mov_b32_e32 v62, v2
	v_mov_b32_e32 v63, v2
	v_mov_b32_e32 v64, v2
	v_mov_b32_e32 v65, v2
	v_mov_b32_e32 v66, v2
	v_mov_b32_e32 v67, v2
	v_mov_b32_e32 v68, v2
	v_mov_b32_e32 v69, v2
	v_mov_b32_e32 v70, v2
	v_mov_b32_e32 v71, v2
	v_mov_b32_e32 v72, v2
	v_mov_b32_e32 v73, v2
	v_mov_b32_e32 v82, v2
	v_mov_b32_e32 v83, v2
	v_mov_b32_e32 v84, v2
	v_mov_b32_e32 v85, v2
	v_mov_b32_e32 v86, v2
	v_mov_b32_e32 v87, v2
	v_mov_b32_e32 v88, v2
	v_mov_b32_e32 v89, v2
	v_mov_b32_e32 v100, v2
	v_mov_b32_e32 v101, v2
	v_mov_b32_e32 v102, v2
	v_mov_b32_e32 v103, v2
	v_mov_b32_e32 v104, v2
	v_mov_b32_e32 v105, v2
	v_mov_b32_e32 v106, v2
	v_mov_b32_e32 v107, v2
	v_mov_b32_e32 v116, v2
	v_mov_b32_e32 v117, v2
	v_mov_b32_e32 v118, v2
	v_mov_b32_e32 v119, v2
	v_mov_b32_e32 v124, v2
	v_mov_b32_e32 v125, v2
	v_mov_b32_e32 v126, v2
	v_mov_b32_e32 v127, v2
	v_mov_b32_e32 v74, v2
	v_mov_b32_e32 v75, v2
	v_mov_b32_e32 v76, v2
	v_mov_b32_e32 v77, v2
	v_mov_b32_e32 v78, v2
	v_mov_b32_e32 v79, v2
	v_mov_b32_e32 v80, v2
	v_mov_b32_e32 v81, v2
	v_mov_b32_e32 v90, v2
	v_mov_b32_e32 v91, v2
	v_mov_b32_e32 v92, v2
	v_mov_b32_e32 v93, v2
	v_mov_b32_e32 v94, v2
	v_mov_b32_e32 v95, v2
	v_mov_b32_e32 v96, v2
	v_mov_b32_e32 v97, v2
	v_mov_b32_e32 v108, v2
	v_mov_b32_e32 v109, v2
	v_mov_b32_e32 v110, v2
	v_mov_b32_e32 v111, v2
	v_mov_b32_e32 v112, v2
	v_mov_b32_e32 v113, v2
	v_mov_b32_e32 v114, v2
	v_mov_b32_e32 v115, v2
	v_mov_b32_e32 v120, v2
	v_mov_b32_e32 v121, v2
	v_mov_b32_e32 v122, v2
	v_mov_b32_e32 v123, v2
	v_mov_b32_e32 v128, v2
	v_mov_b32_e32 v129, v2
	v_mov_b32_e32 v130, v2
	v_mov_b32_e32 v131, v2
	.p2align	6

.LBB0_2237:
	s_add_i32 s19, s8, -2
	s_add_u32 s33, s28, 0x100
	s_addc_u32 s45, s29, 0
	s_mov_b32 s30, 0
	v_mov_b32_e32 v2, 0
	v_mov_b32_e32 v3, 0
	v_mov_b32_e32 v4, 0
	v_mov_b32_e32 v5, 0
	v_mov_b32_e32 v6, 0
	v_mov_b32_e32 v7, 0
	v_mov_b32_e32 v8, 0
	v_mov_b32_e32 v9, 0
	v_mov_b32_e32 v10, 0
	v_mov_b32_e32 v11, 0
	v_mov_b32_e32 v12, 0
	v_mov_b32_e32 v13, 0
	v_mov_b32_e32 v14, 0
	v_mov_b32_e32 v15, 0
	v_mov_b32_e32 v16, 0
	v_mov_b32_e32 v17, 0
	v_mov_b32_e32 v18, 0
	v_mov_b32_e32 v19, 0
	v_mov_b32_e32 v20, 0
	v_mov_b32_e32 v21, 0
	v_mov_b32_e32 v22, 0
	v_mov_b32_e32 v23, 0
	v_mov_b32_e32 v24, 0
	v_mov_b32_e32 v25, 0
	v_mov_b32_e32 v26, 0
	v_mov_b32_e32 v27, 0
	v_mov_b32_e32 v28, 0
	v_mov_b32_e32 v29, 0
	v_mov_b32_e32 v30, 0
	v_mov_b32_e32 v31, 0
	v_mov_b32_e32 v32, 0
	v_mov_b32_e32 v33, 0
	v_mov_b32_e32 v34, 0
	v_mov_b32_e32 v35, 0
	v_mov_b32_e32 v36, 0
	v_mov_b32_e32 v37, 0
	v_mov_b32_e32 v38, 0
	v_mov_b32_e32 v39, 0
	v_mov_b32_e32 v40, 0
	v_mov_b32_e32 v41, 0
	v_mov_b32_e32 v42, 0
	v_mov_b32_e32 v43, 0
	v_mov_b32_e32 v44, 0
	v_mov_b32_e32 v45, 0
	v_mov_b32_e32 v46, 0
	v_mov_b32_e32 v47, 0
	v_mov_b32_e32 v48, 0
	v_mov_b32_e32 v49, 0
	v_mov_b32_e32 v50, 0
	v_mov_b32_e32 v51, 0
	v_mov_b32_e32 v52, 0
	v_mov_b32_e32 v53, 0
	v_mov_b32_e32 v54, 0
	v_mov_b32_e32 v55, 0
	v_mov_b32_e32 v56, 0
	v_mov_b32_e32 v57, 0
	v_mov_b32_e32 v58, 0
	v_mov_b32_e32 v59, 0
	v_mov_b32_e32 v60, 0
	v_mov_b32_e32 v61, 0
	v_mov_b32_e32 v62, 0
	v_mov_b32_e32 v63, 0
	v_mov_b32_e32 v64, 0
	v_mov_b32_e32 v65, 0
	v_mov_b32_e32 v66, 0
	v_mov_b32_e32 v67, 0
	v_mov_b32_e32 v68, 0
	v_mov_b32_e32 v69, 0
	v_mov_b32_e32 v70, 0
	v_mov_b32_e32 v71, 0
	v_mov_b32_e32 v72, 0
	v_mov_b32_e32 v73, 0
	v_mov_b32_e32 v74, 0
	v_mov_b32_e32 v75, 0
	v_mov_b32_e32 v76, 0
	v_mov_b32_e32 v77, 0
	v_mov_b32_e32 v78, 0
	v_mov_b32_e32 v79, 0
	v_mov_b32_e32 v80, 0
	v_mov_b32_e32 v81, 0
	v_mov_b32_e32 v82, 0
	v_mov_b32_e32 v83, 0
	v_mov_b32_e32 v84, 0
	v_mov_b32_e32 v85, 0
	v_mov_b32_e32 v86, 0
	v_mov_b32_e32 v87, 0
	v_mov_b32_e32 v88, 0
	v_mov_b32_e32 v89, 0
	v_mov_b32_e32 v90, 0
	v_mov_b32_e32 v91, 0
	v_mov_b32_e32 v92, 0
	v_mov_b32_e32 v93, 0
	v_mov_b32_e32 v94, 0
	v_mov_b32_e32 v95, 0
	v_mov_b32_e32 v96, 0
	v_mov_b32_e32 v97, 0
	v_mov_b32_e32 v100, 0
	v_mov_b32_e32 v101, 0
	v_mov_b32_e32 v102, 0
	v_mov_b32_e32 v103, 0
	v_mov_b32_e32 v104, 0
	v_mov_b32_e32 v105, 0
	v_mov_b32_e32 v106, 0
	v_mov_b32_e32 v107, 0
	v_mov_b32_e32 v108, 0
	v_mov_b32_e32 v109, 0
	v_mov_b32_e32 v110, 0
	v_mov_b32_e32 v111, 0
	v_mov_b32_e32 v112, 0
	v_mov_b32_e32 v113, 0
	v_mov_b32_e32 v114, 0
	v_mov_b32_e32 v115, 0
	v_mov_b32_e32 v116, 0
	v_mov_b32_e32 v117, 0
	v_mov_b32_e32 v118, 0
	v_mov_b32_e32 v119, 0
	v_mov_b32_e32 v120, 0
	v_mov_b32_e32 v121, 0
	v_mov_b32_e32 v122, 0
	v_mov_b32_e32 v123, 0
	v_mov_b32_e32 v124, 0
	v_mov_b32_e32 v125, 0
	v_mov_b32_e32 v126, 0
	v_mov_b32_e32 v127, 0
	v_mov_b32_e32 v128, 0
	v_mov_b32_e32 v129, 0
	v_mov_b32_e32 v130, 0
	v_mov_b32_e32 v131, 0
	.p2align	6
